# v11 + nt on piggyback loads and stores
# speedup vs baseline: 1.0463x; 1.0048x over previous
; #define PG8_STAGE(bufoff, gbase, v0, v1) do { \
;         __builtin_amdgcn_global_load_lds((const unsigned*)((const char*)(gbase) + (v0)), (LAS unsigned*)(lds + (bufoff) + ldsw), 16, 0, 0); \
;         __builtin_amdgcn_global_load_lds((const unsigned*)((const char*)(gbase) + (v1)), (LAS unsigned*)(lds + (bufoff) + ldsw + 8192), 16, 0, 0); } while (0)
; #define PG8_LDA(dst, b, h) do { _Pragma("unroll") for (int m = 0; m < 4; ++m) _Pragma("unroll") for (int k = 0; k < 2; ++k) dst[m][k] = *(const LAS bf16x8*)(lds + PG8_SA(b, h) + aoff + m * 2048 + k * 1024); } while (0)
; #define PG8_LDB(dst, b, h) do { _Pragma("unroll") for (int n = 0; n < 2; ++n) _Pragma("unroll") for (int k = 0; k < 2; ++k) dst[n][k] = *(const LAS bf16x8*)(lds + PG8_SB(b, h) + boff + n * 2048 + k * 1024); } while (0)
; #define PG8_MMA(ai, bj, At, Bt) do { __builtin_amdgcn_s_setprio(1); _Pragma("unroll") for (int m = 0; m < 4; ++m) _Pragma("unroll") for (int n = 0; n < 2; ++n) _Pragma("unroll") for (int k = 0; k < 2; ++k) \
;         acc[ai][bj][m][n] = __builtin_amdgcn_mfma_f32_16x16x32_bf16(Bt[n][k], At[m][k], acc[ai][bj][m][n], 0, 0, 0); __builtin_amdgcn_s_setprio(0); } while (0)
; #define PG8_WAIT_V(n) asm volatile("s_waitcnt vmcnt(" #n ")" ::: "memory")
; #define PG8_WAIT_L(n) asm volatile("s_waitcnt lgkmcnt(" #n ")" ::: "memory")
; #define PG8_BAR __builtin_amdgcn_s_barrier()
; #define PG8_SCHED __builtin_amdgcn_sched_barrier(0)
; template <class Epi, class Sched>
; __device__ __forceinline__ void gemm_phase(LAS unsigned char* lds, const int K, const Sched& S, const Epi& E) {
;     ...
;             PG8_LDB(B0, 0, 0); PG8_SCHED; PG8_LDA(At, 0, 0); PG8_STAGE(PG8_SA(1, 1), a1, c10, c11);
;             PG8_WAIT_L(8); PG8_BAR; PG8_WAIT_L(0); PG8_MMA(0, 0, At, B0); PG8_BAR; PG8_SCHED;
;             PG8_LDB(B1, 0, 1); PG8_STAGE(PG8_SB(0, 0), b2, voffB0, voffB1);
;             PG8_BAR; PG8_WAIT_L(0); PG8_MMA(0, 1, At, B1); PG8_BAR;
;             PG8_LDA(At, 0, 1); PG8_STAGE(PG8_SA(0, 0), a2, x00, x01);
;             PG8_BAR; PG8_WAIT_L(0); PG8_MMA(1, 0, At, B0); PG8_BAR; PG8_SCHED;
;             PG8_STAGE(PG8_SB(0, 1), b2 + hstep, voffB0, voffB1);
;             PG8_WAIT_V(6); PG8_BAR; PG8_MMA(1, 1, At, B1); PG8_BAR;
.LBB0_1094:
	v_add_u32_e32 v139, s46, v149
	s_add_u32 s22, s0, s20
	ds_read_b128 v[160:163], v139
	ds_read_b128 v[164:167], v139 offset:1024
	ds_read_b128 v[168:171], v139 offset:2048
	ds_read_b128 v[172:175], v139 offset:3072
	s_addc_u32 s23, s1, s21
	s_add_u32 s24, s22, 0x34c30100
	s_addc_u32 s25, s23, 0
	s_cmpk_eq_i32 s20, 0xf00
	s_cselect_b64 vcc, -1, 0
	s_and_b64 s[22:23], vcc, exec
	v_cndmask_b32_e32 v134, v158, v156, vcc
	s_cselect_b32 s27, s3, s25
	s_cselect_b32 s26, s2, s24
	v_cndmask_b32_e32 v139, v138, v154, vcc
	s_cselect_b32 s23, s19, s15
	s_cselect_b32 s22, s18, s13
	v_cndmask_b32_e32 v204, v136, v155, vcc
	s_add_u32 s24, s22, 0x20000
	s_addc_u32 s25, s23, 0
	v_lshl_add_u64 v[206:207], v[144:145], 0, s[20:21]
	s_add_i32 m0, s37, 0xc000
	ds_read_b128 v[176:179], v151
	ds_read_b128 v[180:183], v151 offset:1024
	ds_read_b128 v[184:187], v151 offset:2048
	ds_read_b128 v[188:191], v151 offset:3072
	ds_read_b128 v[192:195], v151 offset:4096
	ds_read_b128 v[196:199], v151 offset:5120
	ds_read_b128 v[200:203], v151 offset:6144
	ds_read_b128 v[208:211], v151 offset:7168
	global_load_lds_dwordx4 v[206:207], off
	v_lshl_add_u64 v[206:207], v[142:143], 0, s[20:21]
	s_add_i32 m0, s37, 0xe000
	s_nop 0
	global_load_lds_dwordx4 v[206:207], off
	s_waitcnt lgkmcnt(8)
	s_barrier
	s_waitcnt lgkmcnt(0)
	s_setprio 1
	s_waitcnt lgkmcnt(0)
	v_mfma_f32_16x16x32_bf16 v[126:129], v[160:163], v[176:179], v[126:129]
	v_mfma_f32_16x16x32_bf16 v[122:125], v[168:171], v[176:179], v[122:125]
	v_mfma_f32_16x16x32_bf16 v[110:113], v[160:163], v[184:187], v[110:113]
	v_mfma_f32_16x16x32_bf16 v[106:109], v[168:171], v[184:187], v[106:109]
	v_mfma_f32_16x16x32_bf16 v[94:97], v[160:163], v[192:195], v[94:97]
	v_mfma_f32_16x16x32_bf16 v[90:93], v[168:171], v[192:195], v[90:93]
	v_mfma_f32_16x16x32_bf16 v[78:81], v[160:163], v[200:203], v[78:81]
	v_mfma_f32_16x16x32_bf16 v[74:77], v[168:171], v[200:203], v[74:77]
	v_mfma_f32_16x16x32_bf16 v[126:129], v[164:167], v[180:183], v[126:129]
	v_mfma_f32_16x16x32_bf16 v[122:125], v[172:175], v[180:183], v[122:125]
	v_mfma_f32_16x16x32_bf16 v[110:113], v[164:167], v[188:191], v[110:113]
	v_mfma_f32_16x16x32_bf16 v[106:109], v[172:175], v[188:191], v[106:109]
	v_mfma_f32_16x16x32_bf16 v[94:97], v[164:167], v[196:199], v[94:97]
	v_mfma_f32_16x16x32_bf16 v[90:93], v[172:175], v[196:199], v[90:93]
	v_mfma_f32_16x16x32_bf16 v[78:81], v[164:167], v[208:211], v[78:81]
	v_mfma_f32_16x16x32_bf16 v[74:77], v[172:175], v[208:211], v[74:77]
	s_setprio 0
	s_barrier
	s_add_i32 s55, s46, s36
	v_add_u32_e32 v141, s48, v149
	v_lshl_add_u64 v[206:207], s[22:23], 0, v[130:131]
	s_mov_b32 m0, s55
	ds_read_b128 v[212:215], v141
	ds_read_b128 v[216:219], v141 offset:1024
	ds_read_b128 v[220:223], v141 offset:2048
	ds_read_b128 v[224:227], v141 offset:3072
	global_load_lds_dwordx4 v[206:207], off
	v_lshl_add_u64 v[228:229], s[22:23], 0, v[132:133]
	s_add_i32 m0, s55, 0x2000
	s_nop 0
	global_load_lds_dwordx4 v[228:229], off
	s_barrier
	s_waitcnt lgkmcnt(0)
	s_setprio 1
	s_waitcnt lgkmcnt(0)
	v_mfma_f32_16x16x32_bf16 v[118:121], v[212:215], v[176:179], v[118:121]
	v_mfma_f32_16x16x32_bf16 v[114:117], v[220:223], v[176:179], v[114:117]
	v_mfma_f32_16x16x32_bf16 v[102:105], v[212:215], v[184:187], v[102:105]
	v_mfma_f32_16x16x32_bf16 v[98:101], v[220:223], v[184:187], v[98:101]
	v_mfma_f32_16x16x32_bf16 v[86:89], v[212:215], v[192:195], v[86:89]
	v_mfma_f32_16x16x32_bf16 v[82:85], v[220:223], v[192:195], v[82:85]
	v_mfma_f32_16x16x32_bf16 v[70:73], v[212:215], v[200:203], v[70:73]
	v_mfma_f32_16x16x32_bf16 v[66:69], v[220:223], v[200:203], v[66:69]
	v_mfma_f32_16x16x32_bf16 v[118:121], v[216:219], v[180:183], v[118:121]
	v_mfma_f32_16x16x32_bf16 v[114:117], v[224:227], v[180:183], v[114:117]
	v_mfma_f32_16x16x32_bf16 v[102:105], v[216:219], v[188:191], v[102:105]
	v_mfma_f32_16x16x32_bf16 v[98:101], v[224:227], v[188:191], v[98:101]
	v_mfma_f32_16x16x32_bf16 v[86:89], v[216:219], v[196:199], v[86:89]
	v_mfma_f32_16x16x32_bf16 v[82:85], v[224:227], v[196:199], v[82:85]
	v_mfma_f32_16x16x32_bf16 v[70:73], v[216:219], v[208:211], v[70:73]
	v_mfma_f32_16x16x32_bf16 v[66:69], v[224:227], v[208:211], v[66:69]
	s_setprio 0
	s_mov_b32 m0, s37
	s_barrier
	ds_read_b128 v[176:179], v151 offset:16384
	ds_read_b128 v[180:183], v151 offset:17408
	ds_read_b128 v[184:187], v151 offset:18432
	ds_read_b128 v[188:191], v151 offset:19456
	ds_read_b128 v[192:195], v151 offset:20480
	ds_read_b128 v[196:199], v151 offset:21504
	ds_read_b128 v[200:203], v151 offset:22528
	ds_read_b128 v[208:211], v151 offset:23552
	global_load_lds_dwordx4 v134, s[26:27]
	s_mov_b32 m0, s38
	v_mov_b32_e32 v205, v135
	global_load_lds_dwordx4 v204, s[26:27]
	s_barrier
	s_waitcnt lgkmcnt(0)
	v_lshl_add_u64 v[230:231], s[26:27], 0, v[134:135]
	v_lshl_add_u64 v[204:205], s[26:27], 0, v[204:205]
	s_setprio 1
	s_waitcnt lgkmcnt(0)
	v_mfma_f32_16x16x32_bf16 v[62:65], v[160:163], v[176:179], v[62:65]
	v_mfma_f32_16x16x32_bf16 v[58:61], v[168:171], v[176:179], v[58:61]
	v_mfma_f32_16x16x32_bf16 v[46:49], v[160:163], v[184:187], v[46:49]
	v_mfma_f32_16x16x32_bf16 v[42:45], v[168:171], v[184:187], v[42:45]
	v_mfma_f32_16x16x32_bf16 v[30:33], v[160:163], v[192:195], v[30:33]
	v_mfma_f32_16x16x32_bf16 v[26:29], v[168:171], v[192:195], v[26:29]
	v_mfma_f32_16x16x32_bf16 v[14:17], v[160:163], v[200:203], v[14:17]
	v_mfma_f32_16x16x32_bf16 v[10:13], v[168:171], v[200:203], v[10:13]
	v_mfma_f32_16x16x32_bf16 v[62:65], v[164:167], v[180:183], v[62:65]
	v_mfma_f32_16x16x32_bf16 v[58:61], v[172:175], v[180:183], v[58:61]
	v_mfma_f32_16x16x32_bf16 v[46:49], v[164:167], v[188:191], v[46:49]
	v_mfma_f32_16x16x32_bf16 v[42:45], v[172:175], v[188:191], v[42:45]
	v_mfma_f32_16x16x32_bf16 v[30:33], v[164:167], v[196:199], v[30:33]
	v_mfma_f32_16x16x32_bf16 v[26:29], v[172:175], v[196:199], v[26:29]
	v_mfma_f32_16x16x32_bf16 v[14:17], v[164:167], v[208:211], v[14:17]
	v_mfma_f32_16x16x32_bf16 v[10:13], v[172:175], v[208:211], v[10:13]
	s_setprio 0
	s_barrier
	s_add_i32 s55, s48, s36
	v_lshl_add_u64 v[160:161], v[206:207], 0, s[4:5]
	s_mov_b32 m0, s55
	s_nop 0
	global_load_lds_dwordx4 v[160:161], off
	v_lshl_add_u64 v[160:161], v[228:229], 0, s[4:5]
	s_add_i32 m0, s55, 0x2000
	s_nop 0
	global_load_lds_dwordx4 v[160:161], off
	s_cmp_eq_u32 s82, 0
	s_cbranch_scc1 .Lpb8_p4n
	s_waitcnt vmcnt(14)
	v_cvt_pk_bf16_f32 v244, v244, v245
	v_cvt_pk_bf16_f32 v245, v246, v247
	v_cvt_pk_bf16_f32 v246, v248, v249
	v_cvt_pk_bf16_f32 v247, v250, v251
	global_store_dwordx4 v253, v[244:247], s[78:79] nt
	s_mov_b32 s82, 0
	s_waitcnt vmcnt(7)
	s_branch .Lpb8_p4j

; #define PG8_STAGE(bufoff, gbase, v0, v1) do { \
;         __builtin_amdgcn_global_load_lds((const unsigned*)((const char*)(gbase) + (v0)), (LAS unsigned*)(lds + (bufoff) + ldsw), 16, 0, 0); \
;         __builtin_amdgcn_global_load_lds((const unsigned*)((const char*)(gbase) + (v1)), (LAS unsigned*)(lds + (bufoff) + ldsw + 8192), 16, 0, 0); } while (0)
; #define PG8_LDA(dst, b, h) do { _Pragma("unroll") for (int m = 0; m < 4; ++m) _Pragma("unroll") for (int k = 0; k < 2; ++k) dst[m][k] = *(const LAS bf16x8*)(lds + PG8_SA(b, h) + aoff + m * 2048 + k * 1024); } while (0)
; #define PG8_LDB(dst, b, h) do { _Pragma("unroll") for (int n = 0; n < 2; ++n) _Pragma("unroll") for (int k = 0; k < 2; ++k) dst[n][k] = *(const LAS bf16x8*)(lds + PG8_SB(b, h) + boff + n * 2048 + k * 1024); } while (0)
; #define PG8_MMA(ai, bj, At, Bt) do { __builtin_amdgcn_s_setprio(1); _Pragma("unroll") for (int m = 0; m < 4; ++m) _Pragma("unroll") for (int n = 0; n < 2; ++n) _Pragma("unroll") for (int k = 0; k < 2; ++k) \
;         acc[ai][bj][m][n] = __builtin_amdgcn_mfma_f32_16x16x32_bf16(Bt[n][k], At[m][k], acc[ai][bj][m][n], 0, 0, 0); __builtin_amdgcn_s_setprio(0); } while (0)
; #define PG8_WAIT_V(n) asm volatile("s_waitcnt vmcnt(" #n ")" ::: "memory")
; #define PG8_BAR __builtin_amdgcn_s_barrier()
; #define PG8_SCHED __builtin_amdgcn_sched_barrier(0)
; template <class Epi, class Sched>
; __device__ __forceinline__ void gemm_phase(LAS unsigned char* lds, const int K, const Sched& S, const Epi& E) {
;     ...
;             PG8_WAIT_V(6); PG8_BAR; PG8_MMA(1, 1, At, B1); PG8_BAR;
;             PG8_LDB(B0, 1, 0); PG8_SCHED; PG8_LDA(At, 1, 0); PG8_STAGE(PG8_SA(0, 1), a2, x10, x11);
.Lpb8_p4j:
	s_barrier
	s_setprio 1
	v_mfma_f32_16x16x32_bf16 v[54:57], v[212:215], v[176:179], v[54:57]
	v_mfma_f32_16x16x32_bf16 v[50:53], v[220:223], v[176:179], v[50:53]
	v_mfma_f32_16x16x32_bf16 v[38:41], v[212:215], v[184:187], v[38:41]
	v_mfma_f32_16x16x32_bf16 v[34:37], v[220:223], v[184:187], v[34:37]
	v_mfma_f32_16x16x32_bf16 v[22:25], v[212:215], v[192:195], v[22:25]
	v_mfma_f32_16x16x32_bf16 v[18:21], v[220:223], v[192:195], v[18:21]
	v_mfma_f32_16x16x32_bf16 v[6:9], v[212:215], v[200:203], v[6:9]
	v_mfma_f32_16x16x32_bf16 v[2:5], v[220:223], v[200:203], v[2:5]
	v_mfma_f32_16x16x32_bf16 v[54:57], v[216:219], v[180:183], v[54:57]
	v_mfma_f32_16x16x32_bf16 v[50:53], v[224:227], v[180:183], v[50:53]
	v_mfma_f32_16x16x32_bf16 v[38:41], v[216:219], v[188:191], v[38:41]
	v_mfma_f32_16x16x32_bf16 v[34:37], v[224:227], v[188:191], v[34:37]
	v_mfma_f32_16x16x32_bf16 v[22:25], v[216:219], v[196:199], v[22:25]
	v_mfma_f32_16x16x32_bf16 v[18:21], v[224:227], v[196:199], v[18:21]
	v_mfma_f32_16x16x32_bf16 v[6:9], v[216:219], v[208:211], v[6:9]
	v_mfma_f32_16x16x32_bf16 v[2:5], v[224:227], v[208:211], v[2:5]
	s_setprio 0
	s_add_i32 s55, 0, 0x18000
	v_add_u32_e32 v134, s55, v149
	s_barrier
	ds_read_b128 v[160:163], v134
	ds_read_b128 v[164:167], v134 offset:1024
	ds_read_b128 v[168:171], v134 offset:2048
	ds_read_b128 v[172:175], v134 offset:3072
	s_mov_b32 m0, s39
	ds_read_b128 v[176:179], v151 offset:32768
	ds_read_b128 v[180:183], v151 offset:33792
	ds_read_b128 v[184:187], v151 offset:34816
	ds_read_b128 v[188:191], v151 offset:35840
	ds_read_b128 v[192:195], v151 offset:36864
	ds_read_b128 v[196:199], v151 offset:37888
	ds_read_b128 v[200:203], v151 offset:38912
	ds_read_b128 v[208:211], v151 offset:39936
	v_cndmask_b32_e32 v134, v140, v153, vcc
	global_load_lds_dwordx4 v139, s[26:27]
	s_mov_b32 m0, s40
	s_nop 0
	global_load_lds_dwordx4 v134, s[26:27]
	s_cmp_ge_u32 s70, 0x28000
	s_cbranch_scc1 .Lpb8_p5n
	s_cmp_eq_u32 s80, 0
	s_cbranch_scc0 .Lpb8_adv2
	s_cmp_ge_u32 s70, 0x18000
	s_cselect_b32 s84, 0x18000, 0
	s_cselect_b32 s83, 0x10000000, 0
	s_mov_b32 s81, 0x4030000
	s_cselect_b32 s81, 0x14430000, s81
	s_sub_u32 s84, s70, s84
	s_lshr_b32 s85, s84, 2
	s_lshl_b32 s85, s85, 14
	s_and_b32 s86, s84, 1
	s_lshl_b32 s87, s86, 10
	s_add_u32 s87, s87, s85
	s_add_u32 s87, s87, s83
	s_bitcmp1_b32 s84, 1
	s_cselect_b64 s[72:73], s[76:77], s[74:75]
	s_add_u32 s72, s72, s87
	s_addc_u32 s73, s73, 0
	s_add_u32 s88, s72, 0x2000
	s_addc_u32 s89, s73, 0
	s_lshl_b32 s86, s86, 13
	s_add_u32 s85, s85, s86
	s_and_b32 s86, s84, 2
	s_lshl_b32 s86, s86, 10
	s_add_u32 s85, s85, s86
	s_add_u32 s85, s85, s81
	v_add_u32_e32 v253, s85, v252
	s_movk_i32 s81, 0x400
	s_branch .Lpb8_ld2

; #define PG8_STAGE(bufoff, gbase, v0, v1) do { \
;         __builtin_amdgcn_global_load_lds((const unsigned*)((const char*)(gbase) + (v0)), (LAS unsigned*)(lds + (bufoff) + ldsw), 16, 0, 0); \
;         __builtin_amdgcn_global_load_lds((const unsigned*)((const char*)(gbase) + (v1)), (LAS unsigned*)(lds + (bufoff) + ldsw + 8192), 16, 0, 0); } while (0)
; #define PG8_LDA(dst, b, h) do { _Pragma("unroll") for (int m = 0; m < 4; ++m) _Pragma("unroll") for (int k = 0; k < 2; ++k) dst[m][k] = *(const LAS bf16x8*)(lds + PG8_SA(b, h) + aoff + m * 2048 + k * 1024); } while (0)
; #define PG8_LDB(dst, b, h) do { _Pragma("unroll") for (int n = 0; n < 2; ++n) _Pragma("unroll") for (int k = 0; k < 2; ++k) dst[n][k] = *(const LAS bf16x8*)(lds + PG8_SB(b, h) + boff + n * 2048 + k * 1024); } while (0)
; #define PG8_MMA(ai, bj, At, Bt) do { __builtin_amdgcn_s_setprio(1); _Pragma("unroll") for (int m = 0; m < 4; ++m) _Pragma("unroll") for (int n = 0; n < 2; ++n) _Pragma("unroll") for (int k = 0; k < 2; ++k) \
;         acc[ai][bj][m][n] = __builtin_amdgcn_mfma_f32_16x16x32_bf16(Bt[n][k], At[m][k], acc[ai][bj][m][n], 0, 0, 0); __builtin_amdgcn_s_setprio(0); } while (0)
; #define PG8_WAIT_L(n) asm volatile("s_waitcnt lgkmcnt(" #n ")" ::: "memory")
; #define PG8_BAR __builtin_amdgcn_s_barrier()
; #define PG8_SCHED __builtin_amdgcn_sched_barrier(0)
; template <class Epi, class Sched>
; __device__ __forceinline__ void gemm_phase(LAS unsigned char* lds, const int K, const Sched& S, const Epi& E) {
;     ...
;             PG8_WAIT_L(8); PG8_BAR; PG8_WAIT_L(0); PG8_MMA(0, 0, At, B0); PG8_BAR; PG8_SCHED;
;             PG8_LDB(B1, 1, 1); PG8_STAGE(PG8_SB(1, 0), b3, voffB0, voffB1);
;             PG8_BAR; PG8_WAIT_L(0); PG8_MMA(0, 1, At, B1); PG8_BAR;
;             PG8_LDA(At, 1, 1); PG8_STAGE(PG8_SA(1, 0), a3, x00, x01);
;             PG8_BAR; PG8_WAIT_L(0); PG8_MMA(1, 0, At, B0); PG8_BAR; PG8_SCHED;
;             PG8_STAGE(PG8_SB(1, 1), b3 + hstep, voffB0, voffB1);
.Lpb8_ld2:
	global_load_dword v244, v238, s[72:73] nt
	global_load_dword v245, v239, s[72:73] nt
	global_load_dword v246, v240, s[72:73] nt
	global_load_dword v247, v241, s[72:73] nt
	global_load_dword v248, v238, s[88:89] nt
	global_load_dword v249, v239, s[88:89] nt
	global_load_dword v250, v240, s[88:89] nt
	global_load_dword v251, v241, s[88:89] nt
	s_add_u32 s80, s80, 1
	s_and_b32 s80, s80, 3
	s_cmp_eq_u32 s80, 0
	s_cselect_b32 s84, s71, 0
	s_add_u32 s70, s70, s84
	s_mov_b32 s82, 1
.Lpb8_p5n:
	s_waitcnt lgkmcnt(8)
	s_barrier
	s_waitcnt lgkmcnt(0)
	s_setprio 1
	s_waitcnt lgkmcnt(0)
	v_mfma_f32_16x16x32_bf16 v[126:129], v[160:163], v[176:179], v[126:129]
	v_mfma_f32_16x16x32_bf16 v[122:125], v[168:171], v[176:179], v[122:125]
	v_mfma_f32_16x16x32_bf16 v[110:113], v[160:163], v[184:187], v[110:113]
	v_mfma_f32_16x16x32_bf16 v[106:109], v[168:171], v[184:187], v[106:109]
	v_mfma_f32_16x16x32_bf16 v[94:97], v[160:163], v[192:195], v[94:97]
	v_mfma_f32_16x16x32_bf16 v[90:93], v[168:171], v[192:195], v[90:93]
	v_mfma_f32_16x16x32_bf16 v[78:81], v[160:163], v[200:203], v[78:81]
	v_mfma_f32_16x16x32_bf16 v[74:77], v[168:171], v[200:203], v[74:77]
	v_mfma_f32_16x16x32_bf16 v[126:129], v[164:167], v[180:183], v[126:129]
	v_mfma_f32_16x16x32_bf16 v[122:125], v[172:175], v[180:183], v[122:125]
	v_mfma_f32_16x16x32_bf16 v[110:113], v[164:167], v[188:191], v[110:113]
	v_mfma_f32_16x16x32_bf16 v[106:109], v[172:175], v[188:191], v[106:109]
	v_mfma_f32_16x16x32_bf16 v[94:97], v[164:167], v[196:199], v[94:97]
	v_mfma_f32_16x16x32_bf16 v[90:93], v[172:175], v[196:199], v[90:93]
	v_mfma_f32_16x16x32_bf16 v[78:81], v[164:167], v[208:211], v[78:81]
	v_mfma_f32_16x16x32_bf16 v[74:77], v[172:175], v[208:211], v[74:77]
	s_setprio 0
	s_barrier
	s_add_i32 s26, 0, 0x1c000
	s_add_i32 s27, s55, s36
	v_add_u32_e32 v134, s26, v149
	v_lshl_add_u64 v[206:207], s[24:25], 0, v[130:131]
	s_mov_b32 m0, s27
	ds_read_b128 v[212:215], v134
	ds_read_b128 v[216:219], v134 offset:1024
	ds_read_b128 v[220:223], v134 offset:2048
	ds_read_b128 v[224:227], v134 offset:3072
	global_load_lds_dwordx4 v[206:207], off
	v_lshl_add_u64 v[206:207], s[24:25], 0, v[132:133]
	s_add_i32 m0, s27, 0x2000
	s_nop 0
	global_load_lds_dwordx4 v[206:207], off
	s_barrier
	s_waitcnt lgkmcnt(0)
	s_setprio 1
	s_waitcnt lgkmcnt(0)
	v_mfma_f32_16x16x32_bf16 v[118:121], v[212:215], v[176:179], v[118:121]
	v_mfma_f32_16x16x32_bf16 v[114:117], v[220:223], v[176:179], v[114:117]
	v_mfma_f32_16x16x32_bf16 v[102:105], v[212:215], v[184:187], v[102:105]
	v_mfma_f32_16x16x32_bf16 v[98:101], v[220:223], v[184:187], v[98:101]
	v_mfma_f32_16x16x32_bf16 v[86:89], v[212:215], v[192:195], v[86:89]
	v_mfma_f32_16x16x32_bf16 v[82:85], v[220:223], v[192:195], v[82:85]
	v_mfma_f32_16x16x32_bf16 v[70:73], v[212:215], v[200:203], v[70:73]
	v_mfma_f32_16x16x32_bf16 v[66:69], v[220:223], v[200:203], v[66:69]
	v_mfma_f32_16x16x32_bf16 v[118:121], v[216:219], v[180:183], v[118:121]
	v_mfma_f32_16x16x32_bf16 v[114:117], v[224:227], v[180:183], v[114:117]
	v_mfma_f32_16x16x32_bf16 v[102:105], v[216:219], v[188:191], v[102:105]
	v_mfma_f32_16x16x32_bf16 v[98:101], v[224:227], v[188:191], v[98:101]
	v_mfma_f32_16x16x32_bf16 v[86:89], v[216:219], v[196:199], v[86:89]
	v_mfma_f32_16x16x32_bf16 v[82:85], v[224:227], v[196:199], v[82:85]
	v_mfma_f32_16x16x32_bf16 v[70:73], v[216:219], v[208:211], v[70:73]
	v_mfma_f32_16x16x32_bf16 v[66:69], v[224:227], v[208:211], v[66:69]
	s_setprio 0
	s_mov_b32 m0, s43
	v_lshl_add_u64 v[206:207], v[230:231], 0, s[10:11]
	s_barrier
	ds_read_b128 v[176:179], v151 offset:49152
	ds_read_b128 v[180:183], v151 offset:50176
	ds_read_b128 v[184:187], v151 offset:51200
	ds_read_b128 v[188:191], v151 offset:52224
	ds_read_b128 v[192:195], v151 offset:53248
	ds_read_b128 v[196:199], v151 offset:54272
	ds_read_b128 v[200:203], v151 offset:55296
	ds_read_b128 v[208:211], v151 offset:56320
	global_load_lds_dwordx4 v[206:207], off
	v_lshl_add_u64 v[204:205], v[204:205], 0, s[10:11]
	s_mov_b32 m0, s44
	s_nop 0
	global_load_lds_dwordx4 v[204:205], off
	s_barrier
	s_waitcnt lgkmcnt(0)
	s_setprio 1
	s_waitcnt lgkmcnt(0)
	v_mfma_f32_16x16x32_bf16 v[62:65], v[160:163], v[176:179], v[62:65]
	v_mfma_f32_16x16x32_bf16 v[58:61], v[168:171], v[176:179], v[58:61]
	v_mfma_f32_16x16x32_bf16 v[46:49], v[160:163], v[184:187], v[46:49]
	v_mfma_f32_16x16x32_bf16 v[42:45], v[168:171], v[184:187], v[42:45]
	v_mfma_f32_16x16x32_bf16 v[30:33], v[160:163], v[192:195], v[30:33]
	v_mfma_f32_16x16x32_bf16 v[26:29], v[168:171], v[192:195], v[26:29]
	v_mfma_f32_16x16x32_bf16 v[14:17], v[160:163], v[200:203], v[14:17]
	v_mfma_f32_16x16x32_bf16 v[10:13], v[168:171], v[200:203], v[10:13]
	v_mfma_f32_16x16x32_bf16 v[62:65], v[164:167], v[180:183], v[62:65]
	v_mfma_f32_16x16x32_bf16 v[58:61], v[172:175], v[180:183], v[58:61]
	v_mfma_f32_16x16x32_bf16 v[46:49], v[164:167], v[188:191], v[46:49]
	v_mfma_f32_16x16x32_bf16 v[42:45], v[172:175], v[188:191], v[42:45]
	v_mfma_f32_16x16x32_bf16 v[30:33], v[164:167], v[196:199], v[30:33]
	v_mfma_f32_16x16x32_bf16 v[26:29], v[172:175], v[196:199], v[26:29]
	v_mfma_f32_16x16x32_bf16 v[14:17], v[164:167], v[208:211], v[14:17]
	v_mfma_f32_16x16x32_bf16 v[10:13], v[172:175], v[208:211], v[10:13]
	s_setprio 0
	s_barrier
	s_add_u32 s22, s22, 0x20800
	s_addc_u32 s23, s23, 0
	s_add_i32 s24, s26, s36
	v_lshl_add_u64 v[160:161], s[22:23], 0, v[130:131]
	s_mov_b32 m0, s24
	s_nop 0
	global_load_lds_dwordx4 v[160:161], off
	v_lshl_add_u64 v[160:161], s[22:23], 0, v[132:133]
	s_add_i32 m0, s24, 0x2000
	s_nop 0
	global_load_lds_dwordx4 v[160:161], off
	s_cmp_eq_u32 s82, 0
	s_cbranch_scc1 .Lpb8_p8n
	s_waitcnt vmcnt(14)
	s_branch .Lpb8_p8j

; #define PG8_WAIT_V(n) asm volatile("s_waitcnt vmcnt(" #n ")" ::: "memory")
; #define PG8_BAR __builtin_amdgcn_s_barrier()
; template <class Epi, class Sched>
; __device__ __forceinline__ void gemm_phase(LAS unsigned char* lds, const int K, const Sched& S, const Epi& E) {
;     ...
;     PG8_WAIT_V(0);
;     if (wr == 0) PG8_BAR;
;     PG8_BAR;
.LBB0_1099:
.Lpb8_drain:
	s_cmp_eq_u32 s82, 0
	s_cbranch_scc1 .Lpb8_d1
	s_waitcnt vmcnt(0)
	v_cvt_pk_bf16_f32 v244, v244, v245
	v_cvt_pk_bf16_f32 v245, v246, v247
	v_cvt_pk_bf16_f32 v246, v248, v249
	v_cvt_pk_bf16_f32 v247, v250, v251
	global_store_dwordx4 v253, v[244:247], s[78:79] nt
	s_mov_b32 s82, 0

; #define PG8_WAIT_V(n) asm volatile("s_waitcnt vmcnt(" #n ")" ::: "memory")
; #define PG8_BAR __builtin_amdgcn_s_barrier()
; template <class Epi, class Sched>
; __device__ __forceinline__ void gemm_phase(LAS unsigned char* lds, const int K, const Sched& S, const Epi& E) {
;     ...
;     PG8_WAIT_V(0);
;     if (wr == 0) PG8_BAR;
;     PG8_BAR;
.Lpb8_ld1:
	global_load_dword v244, v238, s[72:73] nt
	global_load_dword v245, v239, s[72:73] nt
	global_load_dword v246, v240, s[72:73] nt
	global_load_dword v247, v241, s[72:73] nt
	global_load_dword v248, v238, s[88:89] nt
	global_load_dword v249, v239, s[88:89] nt
	global_load_dword v250, v240, s[88:89] nt
	global_load_dword v251, v241, s[88:89] nt
	s_add_u32 s80, s80, 1
	s_and_b32 s80, s80, 3
	s_cmp_eq_u32 s80, 0
	s_cselect_b32 s84, s71, 0
	s_add_u32 s70, s70, s84
	s_mov_b32 s82, 1
	s_branch .Lpb8_drain

; __device__ __forceinline__ unsigned cvt_pk_bf16(float lo, float hi) { unsigned r; asm volatile("v_cvt_pk_bf16_f32 %0, %1, %2" : "=v"(r) : "v"(lo), "v"(hi)); return r; }
; #define PG8_STAGE(bufoff, gbase, v0, v1) do { \
;         __builtin_amdgcn_global_load_lds((const unsigned*)((const char*)(gbase) + (v0)), (LAS unsigned*)(lds + (bufoff) + ldsw), 16, 0, 0); \
;         __builtin_amdgcn_global_load_lds((const unsigned*)((const char*)(gbase) + (v1)), (LAS unsigned*)(lds + (bufoff) + ldsw + 8192), 16, 0, 0); } while (0)
; #define PG8_LDA(dst, b, h) do { _Pragma("unroll") for (int m = 0; m < 4; ++m) _Pragma("unroll") for (int k = 0; k < 2; ++k) dst[m][k] = *(const LAS bf16x8*)(lds + PG8_SA(b, h) + aoff + m * 2048 + k * 1024); } while (0)
; #define PG8_WAIT_V(n) asm volatile("s_waitcnt vmcnt(" #n ")" ::: "memory")
; #define PG8_WAIT_L(n) asm volatile("s_waitcnt lgkmcnt(" #n ")" ::: "memory")
; template <class Epi, class Sched>
; __device__ __forceinline__ void gemm_phase(LAS unsigned char* lds, const int K, const Sched& S, const Epi& E) {
;     ...
;             PG8_LDB(B0, 0, 0); PG8_SCHED; PG8_LDA(At, 0, 0); PG8_STAGE(PG8_SA(1, 1), a1, c10, c11);
;             PG8_WAIT_L(8); PG8_BAR; PG8_WAIT_L(0); PG8_MMA(0, 0, At, B0); PG8_BAR; PG8_SCHED;
;             PG8_LDB(B1, 0, 1); PG8_STAGE(PG8_SB(0, 0), b2, voffB0, voffB1);
;             PG8_BAR; PG8_WAIT_L(0); PG8_MMA(0, 1, At, B1); PG8_BAR;
;             PG8_LDA(At, 0, 1); PG8_STAGE(PG8_SA(0, 0), a2, x00, x01);
;             PG8_BAR; PG8_WAIT_L(0); PG8_MMA(1, 0, At, B0); PG8_BAR; PG8_SCHED;
;             PG8_STAGE(PG8_SB(0, 1), b2 + hstep, voffB0, voffB1);
;             PG8_WAIT_V(6); PG8_BAR; PG8_MMA(1, 1, At, B1); PG8_BAR;
; template <int BANK, int WAITN> __device__ __forceinline__ void bg_finish1(BgState& b) {
;     ...
;     if (dst != nullptr) {
; #pragma unroll
;         for (int c = 0; c < 4; ++c) { u32x4 w;
;             w.x = cvt_pk_bf16(b.r[(BANK * 8 + 0) * 4 + c], b.r[(BANK * 8 + 1) * 4 + c]); w.y = cvt_pk_bf16(b.r[(BANK * 8 + 2) * 4 + c], b.r[(BANK * 8 + 3) * 4 + c]);
;             w.z = cvt_pk_bf16(b.r[(BANK * 8 + 4) * 4 + c], b.r[(BANK * 8 + 5) * 4 + c]); w.w = cvt_pk_bf16(b.r[(BANK * 8 + 6) * 4 + c], b.r[(BANK * 8 + 7) * 4 + c]);
;             bf16_t* dp = dst + (c & 1) * 512 + (c >> 1) * b.o2[BANK];
;             asm volatile("global_store_dwordx4 %0, %1, off\n\ts_nop 1" :: "v"(dp), "v"(w) : "memory"); }
.LBB0_1831:
	v_add_u32_e32 v139, s46, v149
	s_add_u32 s22, s0, s20
	ds_read_b128 v[160:163], v139
	ds_read_b128 v[164:167], v139 offset:1024
	ds_read_b128 v[168:171], v139 offset:2048
	ds_read_b128 v[172:175], v139 offset:3072
	s_addc_u32 s23, s1, s21
	s_add_u32 s24, s22, 0x34c30100
	s_addc_u32 s25, s23, 0
	s_cmpk_eq_i32 s20, 0xf00
	s_cselect_b64 vcc, -1, 0
	s_and_b64 s[22:23], vcc, exec
	v_cndmask_b32_e32 v134, v158, v156, vcc
	s_cselect_b32 s27, s3, s25
	s_cselect_b32 s26, s2, s24
	v_cndmask_b32_e32 v139, v138, v154, vcc
	s_cselect_b32 s23, s19, s15
	s_cselect_b32 s22, s18, s13
	v_cndmask_b32_e32 v224, v136, v155, vcc
	s_add_u32 s24, s22, 0x20000
	s_addc_u32 s25, s23, 0
	v_lshl_add_u64 v[208:209], v[144:145], 0, s[20:21]
	s_add_i32 m0, s37, 0xc000
	ds_read_b128 v[176:179], v151
	ds_read_b128 v[180:183], v151 offset:1024
	ds_read_b128 v[184:187], v151 offset:2048
	ds_read_b128 v[188:191], v151 offset:3072
	ds_read_b128 v[192:195], v151 offset:4096
	ds_read_b128 v[196:199], v151 offset:5120
	ds_read_b128 v[200:203], v151 offset:6144
	ds_read_b128 v[204:207], v151 offset:7168
	global_load_lds_dwordx4 v[208:209], off
	v_lshl_add_u64 v[208:209], v[142:143], 0, s[20:21]
	s_add_i32 m0, s37, 0xe000
	s_nop 0
	global_load_lds_dwordx4 v[208:209], off
	s_waitcnt lgkmcnt(8)
	s_barrier
	s_waitcnt lgkmcnt(0)
	s_setprio 1
	s_waitcnt lgkmcnt(0)
	v_mfma_f32_16x16x32_bf16 v[126:129], v[160:163], v[176:179], v[126:129]
	v_mfma_f32_16x16x32_bf16 v[122:125], v[168:171], v[176:179], v[122:125]
	v_mfma_f32_16x16x32_bf16 v[110:113], v[160:163], v[184:187], v[110:113]
	v_mfma_f32_16x16x32_bf16 v[106:109], v[168:171], v[184:187], v[106:109]
	v_mfma_f32_16x16x32_bf16 v[94:97], v[160:163], v[192:195], v[94:97]
	v_mfma_f32_16x16x32_bf16 v[90:93], v[168:171], v[192:195], v[90:93]
	v_mfma_f32_16x16x32_bf16 v[78:81], v[160:163], v[200:203], v[78:81]
	v_mfma_f32_16x16x32_bf16 v[74:77], v[168:171], v[200:203], v[74:77]
	v_mfma_f32_16x16x32_bf16 v[126:129], v[164:167], v[180:183], v[126:129]
	v_mfma_f32_16x16x32_bf16 v[122:125], v[172:175], v[180:183], v[122:125]
	v_mfma_f32_16x16x32_bf16 v[110:113], v[164:167], v[188:191], v[110:113]
	v_mfma_f32_16x16x32_bf16 v[106:109], v[172:175], v[188:191], v[106:109]
	v_mfma_f32_16x16x32_bf16 v[94:97], v[164:167], v[196:199], v[94:97]
	v_mfma_f32_16x16x32_bf16 v[90:93], v[172:175], v[196:199], v[90:93]
	v_mfma_f32_16x16x32_bf16 v[78:81], v[164:167], v[204:207], v[78:81]
	v_mfma_f32_16x16x32_bf16 v[74:77], v[172:175], v[204:207], v[74:77]
	s_setprio 0
	s_barrier
	s_add_i32 s54, s46, s36
	v_add_u32_e32 v141, s48, v149
	v_lshl_add_u64 v[226:227], s[22:23], 0, v[130:131]
	s_mov_b32 m0, s54
	ds_read_b128 v[208:211], v141
	ds_read_b128 v[212:215], v141 offset:1024
	ds_read_b128 v[216:219], v141 offset:2048
	ds_read_b128 v[220:223], v141 offset:3072
	global_load_lds_dwordx4 v[226:227], off
	v_lshl_add_u64 v[228:229], s[22:23], 0, v[132:133]
	s_add_i32 m0, s54, 0x2000
	s_nop 0
	global_load_lds_dwordx4 v[228:229], off
	s_barrier
	s_waitcnt lgkmcnt(0)
	s_setprio 1
	s_waitcnt lgkmcnt(0)
	v_mfma_f32_16x16x32_bf16 v[118:121], v[208:211], v[176:179], v[118:121]
	v_mfma_f32_16x16x32_bf16 v[114:117], v[216:219], v[176:179], v[114:117]
	v_mfma_f32_16x16x32_bf16 v[102:105], v[208:211], v[184:187], v[102:105]
	v_mfma_f32_16x16x32_bf16 v[98:101], v[216:219], v[184:187], v[98:101]
	v_mfma_f32_16x16x32_bf16 v[86:89], v[208:211], v[192:195], v[86:89]
	v_mfma_f32_16x16x32_bf16 v[82:85], v[216:219], v[192:195], v[82:85]
	v_mfma_f32_16x16x32_bf16 v[70:73], v[208:211], v[200:203], v[70:73]
	v_mfma_f32_16x16x32_bf16 v[66:69], v[216:219], v[200:203], v[66:69]
	v_mfma_f32_16x16x32_bf16 v[118:121], v[212:215], v[180:183], v[118:121]
	v_mfma_f32_16x16x32_bf16 v[114:117], v[220:223], v[180:183], v[114:117]
	v_mfma_f32_16x16x32_bf16 v[102:105], v[212:215], v[188:191], v[102:105]
	v_mfma_f32_16x16x32_bf16 v[98:101], v[220:223], v[188:191], v[98:101]
	v_mfma_f32_16x16x32_bf16 v[86:89], v[212:215], v[196:199], v[86:89]
	v_mfma_f32_16x16x32_bf16 v[82:85], v[220:223], v[196:199], v[82:85]
	v_mfma_f32_16x16x32_bf16 v[70:73], v[212:215], v[204:207], v[70:73]
	v_mfma_f32_16x16x32_bf16 v[66:69], v[220:223], v[204:207], v[66:69]
	s_setprio 0
	s_mov_b32 m0, s37
	s_barrier
	ds_read_b128 v[176:179], v151 offset:16384
	ds_read_b128 v[180:183], v151 offset:17408
	ds_read_b128 v[184:187], v151 offset:18432
	ds_read_b128 v[188:191], v151 offset:19456
	ds_read_b128 v[192:195], v151 offset:20480
	ds_read_b128 v[196:199], v151 offset:21504
	ds_read_b128 v[200:203], v151 offset:22528
	ds_read_b128 v[204:207], v151 offset:23552
	global_load_lds_dwordx4 v134, s[26:27]
	s_mov_b32 m0, s38
	v_mov_b32_e32 v225, v135
	global_load_lds_dwordx4 v224, s[26:27]
	s_barrier
	s_waitcnt lgkmcnt(0)
	v_lshl_add_u64 v[230:231], s[26:27], 0, v[134:135]
	v_lshl_add_u64 v[224:225], s[26:27], 0, v[224:225]
	s_setprio 1
	s_waitcnt lgkmcnt(0)
	v_mfma_f32_16x16x32_bf16 v[62:65], v[160:163], v[176:179], v[62:65]
	v_mfma_f32_16x16x32_bf16 v[58:61], v[168:171], v[176:179], v[58:61]
	v_mfma_f32_16x16x32_bf16 v[46:49], v[160:163], v[184:187], v[46:49]
	v_mfma_f32_16x16x32_bf16 v[42:45], v[168:171], v[184:187], v[42:45]
	v_mfma_f32_16x16x32_bf16 v[30:33], v[160:163], v[192:195], v[30:33]
	v_mfma_f32_16x16x32_bf16 v[26:29], v[168:171], v[192:195], v[26:29]
	v_mfma_f32_16x16x32_bf16 v[14:17], v[160:163], v[200:203], v[14:17]
	v_mfma_f32_16x16x32_bf16 v[10:13], v[168:171], v[200:203], v[10:13]
	v_mfma_f32_16x16x32_bf16 v[62:65], v[164:167], v[180:183], v[62:65]
	v_mfma_f32_16x16x32_bf16 v[58:61], v[172:175], v[180:183], v[58:61]
	v_mfma_f32_16x16x32_bf16 v[46:49], v[164:167], v[188:191], v[46:49]
	v_mfma_f32_16x16x32_bf16 v[42:45], v[172:175], v[188:191], v[42:45]
	v_mfma_f32_16x16x32_bf16 v[30:33], v[164:167], v[196:199], v[30:33]
	v_mfma_f32_16x16x32_bf16 v[26:29], v[172:175], v[196:199], v[26:29]
	v_mfma_f32_16x16x32_bf16 v[14:17], v[164:167], v[204:207], v[14:17]
	v_mfma_f32_16x16x32_bf16 v[10:13], v[172:175], v[204:207], v[10:13]
	s_setprio 0
	s_barrier
	s_add_i32 s54, s48, s36
	v_lshl_add_u64 v[160:161], v[226:227], 0, s[4:5]
	s_mov_b32 m0, s54
	s_nop 0
	global_load_lds_dwordx4 v[160:161], off
	v_lshl_add_u64 v[160:161], v[228:229], 0, s[4:5]
	s_add_i32 m0, s54, 0x2000
	s_nop 0
	global_load_lds_dwordx4 v[160:161], off
	s_cmp_eq_u32 s82, 0
	s_cbranch_scc1 .Lpb17_p4n
	s_waitcnt vmcnt(14)
	v_cvt_pk_bf16_f32 v244, v244, v245
	v_cvt_pk_bf16_f32 v245, v246, v247
	v_cvt_pk_bf16_f32 v246, v248, v249
	v_cvt_pk_bf16_f32 v247, v250, v251
	global_store_dwordx4 v253, v[244:247], s[78:79] nt
	s_mov_b32 s82, 0
	s_waitcnt vmcnt(7)
	s_branch .Lpb17_p4j

; #define PG8_STAGE(bufoff, gbase, v0, v1) do { \
;         __builtin_amdgcn_global_load_lds((const unsigned*)((const char*)(gbase) + (v0)), (LAS unsigned*)(lds + (bufoff) + ldsw), 16, 0, 0); \
;         __builtin_amdgcn_global_load_lds((const unsigned*)((const char*)(gbase) + (v1)), (LAS unsigned*)(lds + (bufoff) + ldsw + 8192), 16, 0, 0); } while (0)
; #define PG8_LDA(dst, b, h) do { _Pragma("unroll") for (int m = 0; m < 4; ++m) _Pragma("unroll") for (int k = 0; k < 2; ++k) dst[m][k] = *(const LAS bf16x8*)(lds + PG8_SA(b, h) + aoff + m * 2048 + k * 1024); } while (0)
; #define PG8_LDB(dst, b, h) do { _Pragma("unroll") for (int n = 0; n < 2; ++n) _Pragma("unroll") for (int k = 0; k < 2; ++k) dst[n][k] = *(const LAS bf16x8*)(lds + PG8_SB(b, h) + boff + n * 2048 + k * 1024); } while (0)
; #define PG8_MMA(ai, bj, At, Bt) do { __builtin_amdgcn_s_setprio(1); _Pragma("unroll") for (int m = 0; m < 4; ++m) _Pragma("unroll") for (int n = 0; n < 2; ++n) _Pragma("unroll") for (int k = 0; k < 2; ++k) \
;         acc[ai][bj][m][n] = __builtin_amdgcn_mfma_f32_16x16x32_bf16(Bt[n][k], At[m][k], acc[ai][bj][m][n], 0, 0, 0); __builtin_amdgcn_s_setprio(0); } while (0)
; #define PG8_WAIT_V(n) asm volatile("s_waitcnt vmcnt(" #n ")" ::: "memory")
; #define PG8_BAR __builtin_amdgcn_s_barrier()
; #define PG8_SCHED __builtin_amdgcn_sched_barrier(0)
; template <class Epi, class Sched>
; __device__ __forceinline__ void gemm_phase(LAS unsigned char* lds, const int K, const Sched& S, const Epi& E) {
;     ...
;             PG8_WAIT_V(6); PG8_BAR; PG8_MMA(1, 1, At, B1); PG8_BAR;
;             PG8_LDB(B0, 1, 0); PG8_SCHED; PG8_LDA(At, 1, 0); PG8_STAGE(PG8_SA(0, 1), a2, x10, x11);
; __device__ __forceinline__ bool bg_decode(int st, int wg, int NW, int lane, KP kp, const float*& src, int& ldS, bf16_t*& dst, int& o2) {
;     ...
;     } else {
;         const int r2 = r - 65536, e = r2 >> 9, kc = (r2 >> 3) & 63, cc = r2 & 7, n = cc * 256 + lane;
;         ldS = D; o2 = 128 * 8;
;         src = kp->in[29] + ((size_t)(l * NE + e) * FF + kc * 8) * D + n;
;         dst = (bf16_t*)(ws + WS_WD) + l * WD_L + (size_t)e * D * FF + ((size_t)kc * D + n) * 8;
;     }
.Lpb17_p4j:
	s_barrier
	s_setprio 1
	v_mfma_f32_16x16x32_bf16 v[54:57], v[208:211], v[176:179], v[54:57]
	v_mfma_f32_16x16x32_bf16 v[50:53], v[216:219], v[176:179], v[50:53]
	v_mfma_f32_16x16x32_bf16 v[38:41], v[208:211], v[184:187], v[38:41]
	v_mfma_f32_16x16x32_bf16 v[34:37], v[216:219], v[184:187], v[34:37]
	v_mfma_f32_16x16x32_bf16 v[22:25], v[208:211], v[192:195], v[22:25]
	v_mfma_f32_16x16x32_bf16 v[18:21], v[216:219], v[192:195], v[18:21]
	v_mfma_f32_16x16x32_bf16 v[6:9], v[208:211], v[200:203], v[6:9]
	v_mfma_f32_16x16x32_bf16 v[2:5], v[216:219], v[200:203], v[2:5]
	v_mfma_f32_16x16x32_bf16 v[54:57], v[212:215], v[180:183], v[54:57]
	v_mfma_f32_16x16x32_bf16 v[50:53], v[220:223], v[180:183], v[50:53]
	v_mfma_f32_16x16x32_bf16 v[38:41], v[212:215], v[188:191], v[38:41]
	v_mfma_f32_16x16x32_bf16 v[34:37], v[220:223], v[188:191], v[34:37]
	v_mfma_f32_16x16x32_bf16 v[22:25], v[212:215], v[196:199], v[22:25]
	v_mfma_f32_16x16x32_bf16 v[18:21], v[220:223], v[196:199], v[18:21]
	v_mfma_f32_16x16x32_bf16 v[6:9], v[212:215], v[204:207], v[6:9]
	v_mfma_f32_16x16x32_bf16 v[2:5], v[220:223], v[204:207], v[2:5]
	s_setprio 0
	s_add_i32 s54, 0, 0x18000
	v_add_u32_e32 v134, s54, v149
	s_barrier
	ds_read_b128 v[160:163], v134
	ds_read_b128 v[164:167], v134 offset:1024
	ds_read_b128 v[168:171], v134 offset:2048
	ds_read_b128 v[172:175], v134 offset:3072
	s_mov_b32 m0, s39
	ds_read_b128 v[176:179], v151 offset:32768
	ds_read_b128 v[180:183], v151 offset:33792
	ds_read_b128 v[184:187], v151 offset:34816
	ds_read_b128 v[188:191], v151 offset:35840
	ds_read_b128 v[192:195], v151 offset:36864
	ds_read_b128 v[196:199], v151 offset:37888
	ds_read_b128 v[200:203], v151 offset:38912
	ds_read_b128 v[204:207], v151 offset:39936
	v_cndmask_b32_e32 v134, v140, v153, vcc
	global_load_lds_dwordx4 v139, s[26:27]
	s_mov_b32 m0, s40
	s_nop 0
	global_load_lds_dwordx4 v134, s[26:27]
	s_cmp_ge_u32 s70, 0x30000
	s_cbranch_scc1 .Lpb17_p5n
	s_cmp_eq_u32 s80, 0
	s_cbranch_scc0 .Lpb17_adv4
	s_cmp_ge_u32 s70, 0x28000
	s_mov_b32 s84, 0x10000
	s_cselect_b32 s84, 0x28000, s84
	s_cselect_b32 s83, 0x10000000, 0
	s_mov_b32 s81, 0x24830000
	s_cselect_b32 s81, 0x2ca30000, s81
	s_sub_u32 s84, s70, s84
	s_lshr_b32 s85, s84, 3
	s_and_b32 s86, s84, 7
	s_lshl_b32 s87, s85, 16
	s_lshl_b32 s84, s86, 10
	s_add_u32 s87, s87, s84
	s_add_u32 s87, s87, s83
	s_add_u32 s72, s74, s87
	s_addc_u32 s73, s75, 0
	s_add_u32 s88, s72, 0x8000
	s_addc_u32 s89, s73, 0
	s_lshl_b32 s85, s85, 15
	s_lshl_b32 s86, s86, 12
	s_add_u32 s85, s85, s86
	s_add_u32 s85, s85, s81
	v_add_u32_e32 v253, s85, v252
	s_branch .Lpb17_ld4

; #define PG8_STAGE(bufoff, gbase, v0, v1) do { \
;         __builtin_amdgcn_global_load_lds((const unsigned*)((const char*)(gbase) + (v0)), (LAS unsigned*)(lds + (bufoff) + ldsw), 16, 0, 0); \
;         __builtin_amdgcn_global_load_lds((const unsigned*)((const char*)(gbase) + (v1)), (LAS unsigned*)(lds + (bufoff) + ldsw + 8192), 16, 0, 0); } while (0)
; #define PG8_LDA(dst, b, h) do { _Pragma("unroll") for (int m = 0; m < 4; ++m) _Pragma("unroll") for (int k = 0; k < 2; ++k) dst[m][k] = *(const LAS bf16x8*)(lds + PG8_SA(b, h) + aoff + m * 2048 + k * 1024); } while (0)
; #define PG8_LDB(dst, b, h) do { _Pragma("unroll") for (int n = 0; n < 2; ++n) _Pragma("unroll") for (int k = 0; k < 2; ++k) dst[n][k] = *(const LAS bf16x8*)(lds + PG8_SB(b, h) + boff + n * 2048 + k * 1024); } while (0)
; #define PG8_MMA(ai, bj, At, Bt) do { __builtin_amdgcn_s_setprio(1); _Pragma("unroll") for (int m = 0; m < 4; ++m) _Pragma("unroll") for (int n = 0; n < 2; ++n) _Pragma("unroll") for (int k = 0; k < 2; ++k) \
;         acc[ai][bj][m][n] = __builtin_amdgcn_mfma_f32_16x16x32_bf16(Bt[n][k], At[m][k], acc[ai][bj][m][n], 0, 0, 0); __builtin_amdgcn_s_setprio(0); } while (0)
; #define PG8_WAIT_V(n) asm volatile("s_waitcnt vmcnt(" #n ")" ::: "memory")
; #define PG8_WAIT_L(n) asm volatile("s_waitcnt lgkmcnt(" #n ")" ::: "memory")
; #define PG8_BAR __builtin_amdgcn_s_barrier()
; #define PG8_SCHED __builtin_amdgcn_sched_barrier(0)
; template <class Epi, class Sched>
; __device__ __forceinline__ void gemm_phase(LAS unsigned char* lds, const int K, const Sched& S, const Epi& E) {
;     ...
;             PG8_WAIT_L(8); PG8_BAR; PG8_WAIT_L(0); PG8_MMA(0, 0, At, B0); PG8_BAR; PG8_SCHED;
;             PG8_LDB(B1, 1, 1); PG8_STAGE(PG8_SB(1, 0), b3, voffB0, voffB1);
;             PG8_BAR; PG8_WAIT_L(0); PG8_MMA(0, 1, At, B1); PG8_BAR;
;             PG8_LDA(At, 1, 1); PG8_STAGE(PG8_SA(1, 0), a3, x00, x01);
;             PG8_BAR; PG8_WAIT_L(0); PG8_MMA(1, 0, At, B0); PG8_BAR; PG8_SCHED;
;             PG8_STAGE(PG8_SB(1, 1), b3 + hstep, voffB0, voffB1);
;             PG8_WAIT_V(6); PG8_BAR; PG8_MMA(1, 1, At, B1); PG8_BAR;
.Lpb17_p5n:
	s_waitcnt lgkmcnt(8)
	s_barrier
	s_waitcnt lgkmcnt(0)
	s_setprio 1
	s_waitcnt lgkmcnt(0)
	v_mfma_f32_16x16x32_bf16 v[126:129], v[160:163], v[176:179], v[126:129]
	v_mfma_f32_16x16x32_bf16 v[122:125], v[168:171], v[176:179], v[122:125]
	v_mfma_f32_16x16x32_bf16 v[110:113], v[160:163], v[184:187], v[110:113]
	v_mfma_f32_16x16x32_bf16 v[106:109], v[168:171], v[184:187], v[106:109]
	v_mfma_f32_16x16x32_bf16 v[94:97], v[160:163], v[192:195], v[94:97]
	v_mfma_f32_16x16x32_bf16 v[90:93], v[168:171], v[192:195], v[90:93]
	v_mfma_f32_16x16x32_bf16 v[78:81], v[160:163], v[200:203], v[78:81]
	v_mfma_f32_16x16x32_bf16 v[74:77], v[168:171], v[200:203], v[74:77]
	v_mfma_f32_16x16x32_bf16 v[126:129], v[164:167], v[180:183], v[126:129]
	v_mfma_f32_16x16x32_bf16 v[122:125], v[172:175], v[180:183], v[122:125]
	v_mfma_f32_16x16x32_bf16 v[110:113], v[164:167], v[188:191], v[110:113]
	v_mfma_f32_16x16x32_bf16 v[106:109], v[172:175], v[188:191], v[106:109]
	v_mfma_f32_16x16x32_bf16 v[94:97], v[164:167], v[196:199], v[94:97]
	v_mfma_f32_16x16x32_bf16 v[90:93], v[172:175], v[196:199], v[90:93]
	v_mfma_f32_16x16x32_bf16 v[78:81], v[164:167], v[204:207], v[78:81]
	v_mfma_f32_16x16x32_bf16 v[74:77], v[172:175], v[204:207], v[74:77]
	s_setprio 0
	s_barrier
	s_add_i32 s26, 0, 0x1c000
	s_add_i32 s27, s54, s36
	v_add_u32_e32 v134, s26, v149
	v_lshl_add_u64 v[226:227], s[24:25], 0, v[130:131]
	s_mov_b32 m0, s27
	ds_read_b128 v[208:211], v134
	ds_read_b128 v[212:215], v134 offset:1024
	ds_read_b128 v[216:219], v134 offset:2048
	ds_read_b128 v[220:223], v134 offset:3072
	global_load_lds_dwordx4 v[226:227], off
	v_lshl_add_u64 v[226:227], s[24:25], 0, v[132:133]
	s_add_i32 m0, s27, 0x2000
	s_nop 0
	global_load_lds_dwordx4 v[226:227], off
	s_barrier
	s_waitcnt lgkmcnt(0)
	s_setprio 1
	s_waitcnt lgkmcnt(0)
	v_mfma_f32_16x16x32_bf16 v[118:121], v[208:211], v[176:179], v[118:121]
	v_mfma_f32_16x16x32_bf16 v[114:117], v[216:219], v[176:179], v[114:117]
	v_mfma_f32_16x16x32_bf16 v[102:105], v[208:211], v[184:187], v[102:105]
	v_mfma_f32_16x16x32_bf16 v[98:101], v[216:219], v[184:187], v[98:101]
	v_mfma_f32_16x16x32_bf16 v[86:89], v[208:211], v[192:195], v[86:89]
	v_mfma_f32_16x16x32_bf16 v[82:85], v[216:219], v[192:195], v[82:85]
	v_mfma_f32_16x16x32_bf16 v[70:73], v[208:211], v[200:203], v[70:73]
	v_mfma_f32_16x16x32_bf16 v[66:69], v[216:219], v[200:203], v[66:69]
	v_mfma_f32_16x16x32_bf16 v[118:121], v[212:215], v[180:183], v[118:121]
	v_mfma_f32_16x16x32_bf16 v[114:117], v[220:223], v[180:183], v[114:117]
	v_mfma_f32_16x16x32_bf16 v[102:105], v[212:215], v[188:191], v[102:105]
	v_mfma_f32_16x16x32_bf16 v[98:101], v[220:223], v[188:191], v[98:101]
	v_mfma_f32_16x16x32_bf16 v[86:89], v[212:215], v[196:199], v[86:89]
	v_mfma_f32_16x16x32_bf16 v[82:85], v[220:223], v[196:199], v[82:85]
	v_mfma_f32_16x16x32_bf16 v[70:73], v[212:215], v[204:207], v[70:73]
	v_mfma_f32_16x16x32_bf16 v[66:69], v[220:223], v[204:207], v[66:69]
	s_setprio 0
	s_mov_b32 m0, s43
	v_lshl_add_u64 v[226:227], v[230:231], 0, s[10:11]
	s_barrier
	ds_read_b128 v[176:179], v151 offset:49152
	ds_read_b128 v[180:183], v151 offset:50176
	ds_read_b128 v[184:187], v151 offset:51200
	ds_read_b128 v[188:191], v151 offset:52224
	ds_read_b128 v[192:195], v151 offset:53248
	ds_read_b128 v[196:199], v151 offset:54272
	ds_read_b128 v[200:203], v151 offset:55296
	ds_read_b128 v[204:207], v151 offset:56320
	global_load_lds_dwordx4 v[226:227], off
	v_lshl_add_u64 v[224:225], v[224:225], 0, s[10:11]
	s_mov_b32 m0, s44
	s_nop 0
	global_load_lds_dwordx4 v[224:225], off
	s_barrier
	s_waitcnt lgkmcnt(0)
	s_setprio 1
	s_waitcnt lgkmcnt(0)
	v_mfma_f32_16x16x32_bf16 v[62:65], v[160:163], v[176:179], v[62:65]
	v_mfma_f32_16x16x32_bf16 v[58:61], v[168:171], v[176:179], v[58:61]
	v_mfma_f32_16x16x32_bf16 v[46:49], v[160:163], v[184:187], v[46:49]
	v_mfma_f32_16x16x32_bf16 v[42:45], v[168:171], v[184:187], v[42:45]
	v_mfma_f32_16x16x32_bf16 v[30:33], v[160:163], v[192:195], v[30:33]
	v_mfma_f32_16x16x32_bf16 v[26:29], v[168:171], v[192:195], v[26:29]
	v_mfma_f32_16x16x32_bf16 v[14:17], v[160:163], v[200:203], v[14:17]
	v_mfma_f32_16x16x32_bf16 v[10:13], v[168:171], v[200:203], v[10:13]
	v_mfma_f32_16x16x32_bf16 v[62:65], v[164:167], v[180:183], v[62:65]
	v_mfma_f32_16x16x32_bf16 v[58:61], v[172:175], v[180:183], v[58:61]
	v_mfma_f32_16x16x32_bf16 v[46:49], v[164:167], v[188:191], v[46:49]
	v_mfma_f32_16x16x32_bf16 v[42:45], v[172:175], v[188:191], v[42:45]
	v_mfma_f32_16x16x32_bf16 v[30:33], v[164:167], v[196:199], v[30:33]
	v_mfma_f32_16x16x32_bf16 v[26:29], v[172:175], v[196:199], v[26:29]
	v_mfma_f32_16x16x32_bf16 v[14:17], v[164:167], v[204:207], v[14:17]
	v_mfma_f32_16x16x32_bf16 v[10:13], v[172:175], v[204:207], v[10:13]
	s_setprio 0
	s_barrier
	s_add_u32 s22, s22, 0x20800
	s_addc_u32 s23, s23, 0
	s_add_i32 s24, s26, s36
	v_lshl_add_u64 v[160:161], s[22:23], 0, v[130:131]
	s_mov_b32 m0, s24
	s_nop 0
	global_load_lds_dwordx4 v[160:161], off
	v_lshl_add_u64 v[160:161], s[22:23], 0, v[132:133]
	s_add_i32 m0, s24, 0x2000
	s_nop 0
	global_load_lds_dwordx4 v[160:161], off
	s_cmp_eq_u32 s82, 0
	s_cbranch_scc1 .Lpb17_p8n
	s_waitcnt vmcnt(14)
	s_branch .Lpb17_p8j
